# flattened P1 classes with converter quota 13 (class A quota 4)
# speedup vs baseline: 1.0091x; 1.0091x over previous
; #define LAS __attribute__((address_space(3)))
; template <bool STEAL>
; __device__ __forceinline__ void f8_convert(const Args& a, LAS unsigned char* lds, unsigned char* ws, int l, int first, int stride, int quota, unsigned* ticket, int tid, int lane, int wave) {
;     ...
;     while (k < F8_TILES_PER_LAYER) {
;         LAS unsigned char* buf = lds + (n & 1) * 65536;
;         if constexpr (STEAL) { if (tid == 0) word[(n + 1) & 1] = (n + 1 < quota) ? (int)__hip_atomic_fetch_add(ticket, 1u, __ATOMIC_RELAXED, __HIP_MEMORY_SCOPE_AGENT) : F8_TILES_PER_LAYER; }
.LBB0_247:
	s_and_saveexec_b64 s[2:3], s[0:1]
	s_xor_b64 s[2:3], exec, s[2:3]
	s_and_b32 s4, s35, 1
	s_or_saveexec_b64 s[2:3], s[2:3]
	v_mov_b32_e32 v152, s4
	s_xor_b64 exec, exec, s[2:3]
	s_cbranch_execz .LBB0_253
	v_readlane_b32 s4, v255, 61
	s_nop 0
	s_cmp_eq_u32 s4, 3
	s_cselect_b32 s4, 12, 3
	s_cmp_gt_u32 s35, s4
	v_mov_b32_e32 v152, 0x6e0
	s_cbranch_scc1 .LBB0_252
	v_mov_b64_e32 v[152:153], s[6:7]
	flat_atomic_add v152, v[152:153], v206 sc0
